# grid-barrier poll interval lengthened (s_sleep 10 to 24) to reduce polling traffic while stragglers stream
# speedup vs baseline: 1.0077x; 1.0077x over previous
.LBB1_26:
	s_or_b64 exec, exec, s[12:13]
	v_cndmask_b32_e64 v74, 0, 1, s[16:17]
	v_cmp_ne_u32_e32 vcc, 0, v74
	s_cmp_eq_u64 vcc, exec
	s_cbranch_scc1 .LBB1_23
	s_mov_b64 s[16:17], -1
	s_sleep 24
	s_and_saveexec_b64 s[12:13], s[2:3]
	s_cbranch_execz .LBB1_29
	global_load_dword v74, v[66:67], off sc1
	s_waitcnt vmcnt(0)
	v_cmp_lt_u32_e32 vcc, 31, v74
	s_orn2_b64 s[16:17], vcc, exec

.LBB1_38:
	s_or_b64 exec, exec, s[12:13]
	v_cndmask_b32_e64 v74, 0, 1, s[16:17]
	v_cmp_ne_u32_e32 vcc, 0, v74
	s_cmp_eq_u64 vcc, exec
	s_cbranch_scc1 .LBB1_23
	s_add_i32 s19, s19, 5
	s_cmp_gt_u32 s19, 0x3ffffb
	s_cselect_b64 s[6:7], -1, 0
	s_sleep 24
	s_branch .LBB1_23
